# P4 branch GEMM: start of WGs staggered by XCD&3 (3.4 us steps) so the gate-rescale HBM bursts of XCD groups do not coincide; on top of router loop rewrite
# speedup vs baseline: 1.0018x; 1.0018x over previous
; #define PG8_STAGE_A(bufoff, kptr, h) do { if constexpr (GATHER) { PG8_STAGE(bufoff, kptr, oa[h]); } else { PG8_STAGE(bufoff, (kptr) + (h) * hstep, voffA); } } while (0)
; #define PG8_GATHER_OFFS(uidx) do { _Pragma("unroll") for (int _h = 0; _h < 2; ++_h) _Pragma("unroll") for (int _i = 0; _i < 2; ++_i) \
;         oa[_h][_i] = (unsigned)(S.gather_row((uidx), _h * HALF + _i * 64 + Rst0) * K + Cst0) * 2u; } while (0)
; template <class Epi, class Sched, bool GATHER, bool SEGHOOK = false>
; __device__ __forceinline__ void gemm_phase(LAS unsigned char* lds, const int K, const Sched& S, const Epi& E, int tid_) {
;     ...
;     const int tid = tid_, wid = __builtin_amdgcn_readfirstlane(tid >> 6), lane = tid & 63, wr = wid >> 2, wc = wid & 3, fr = lane & 15, fq = lane >> 4;
;     const int nt = K / BK;
;     unsigned voffA[2], voffB[2];
;     unsigned oa[2][2];
;     const size_t kstep = (size_t)(BK * 2);
;     const size_t hstep = (size_t)HALF * K * 2;
;     int Rst0, Cst0;
;     { int R, C; stage_rc(tid * 16, R, C); Rst0 = R; Cst0 = C; }
; #pragma unroll
;     for (int i = 0; i < 2; ++i) { int R, C; stage_rc(tid * 16 + i * 8192, R, C); const int Rb = Epi::PERM ? ((R & ~31) + perm32(R & 31)) : R;
;         voffA[i] = (unsigned)(R * K + C) * 2u; voffB[i] = (unsigned)(Rb * K + C) * 2u; oa[0][i] = 0u; oa[1][i] = 0u; }
;     ...
;     const unsigned ldsw = (unsigned)wid * 1024u;
;     const int aoff = lds_byte(wr * 64 + fr, fq * 8), boff = lds_byte(wc * 32 + fr, fq * 8);
;     ...
;     Unit cur, nxt; int ui = 0;
;     if (!S.next(0, cur)) return;
;     if constexpr (GATHER) { PG8_GATHER_OFFS(0); }
;     f32x4 acc[2][2][4][2];
; #pragma unroll
;     for (int a = 0; a < 2; ++a)
; #pragma unroll
;         for (int b = 0; b < 2; ++b)
; #pragma unroll
;             for (int m = 0; m < 4; ++m)
; #pragma unroll
;                 for (int n = 0; n < 2; ++n) acc[a][b][m][n] = (f32x4){0.f, 0.f, 0.f, 0.f};
;     bf16x8 At[4][2], B0[2][2], B1[2][2];
;     const char* cA = S.a_base(cur); const char* cB = S.b_base(cur);
;     PG8_STAGE(PG8_SB(0, 0), cB, voffB); PG8_STAGE(PG8_SB(0, 1), cB + hstep, voffB); PG8_STAGE_A(PG8_SA(0, 0), cA, 0); PG8_STAGE_A(PG8_SA(0, 1), cA, 1);
;     if (wr == 1) PG8_BAR;
;     PG8_WAIT_V(2); PG8_BAR;
;     PG8_STAGE(PG8_SB(1, 0), cB + kstep, voffB); PG8_STAGE_A(PG8_SA(1, 0), cA + kstep, 0); PG8_STAGE(PG8_SB(1, 1), cB + hstep + kstep, voffB);
;     PG8_WAIT_V(6); PG8_BAR;
.LBB0_628:
	v_readlane_b32 s2, v249, 5
	v_readlane_b32 s3, v249, 6
	s_cmp_le_i32 s2, s8
	s_cselect_b64 s[2:3], -1, 0
	s_and_b64 s[0:1], s[2:3], s[0:1]
	v_readlane_b32 s2, v248, 23
	v_readlane_b32 s3, v248, 24
	s_andn2_b64 vcc, exec, s[0:1]
	s_nop 0
	v_cndmask_b32_e64 v0, 0, 1, s[2:3]
	v_cmp_ne_u32_e64 s[2:3], 1, v0
	s_nop 1
	v_writelane_b32 v246, s2, 30
	s_nop 1
	v_writelane_b32 v246, s3, 31
	s_cbranch_vccnz .LBB0_663
	s_and_b32 s100, s92, 3
.Lstg_loop_P4:
	s_cmp_eq_u32 s100, 0
	s_cbranch_scc1 .Lstg_done_P4
	s_sleep 127
	s_sub_u32 s100, s100, 1
	s_branch .Lstg_loop_P4
.Lstg_done_P4:
	s_mov_b32 s2, -1
	s_nop 0
	v_mbcnt_lo_u32_b32 v0, s2, 0
	v_mbcnt_hi_u32_b32 v0, s2, v0
	v_readlane_b32 s2, v249, 4
	s_nop 1
	v_add_u32_e32 v0, s2, v0
	v_readlane_b32 s2, v247, 30
	s_waitcnt vmcnt(0) lgkmcnt(0)
	s_nop 0
	v_mov_b32_e32 v2, s2
	ds_read_b64 v[2:3], v2
	v_readlane_b32 s2, v246, 30
	v_readlane_b32 s3, v246, 31
	s_and_b64 vcc, exec, s[2:3]
	s_waitcnt lgkmcnt(0)
	v_readfirstlane_b32 s28, v2
	v_readfirstlane_b32 s29, v3
	v_readfirstlane_b32 s2, v0
	s_cbranch_vccnz .LBB0_663
	v_lshlrev_b32_e32 v2, 4, v0
	v_add_u32_e32 v3, 0x2000, v2
	v_ashrrev_i32_e32 v4, 31, v3
	v_lshrrev_b32_e32 v4, 22, v4
	v_add_u32_e32 v4, v3, v4
	v_ashrrev_i32_e32 v4, 10, v4
	v_mul_i32_i24_e32 v5, 0x400, v4
	v_sub_u32_e32 v3, v3, v5
	v_lshrrev_b32_e32 v5, 4, v3
	v_bitop3_b32 v3, v5, v3, 32 bitop3:0x6c
	v_ashrrev_i32_e32 v5, 31, v3
	v_lshrrev_b32_e32 v5, 26, v5
	s_add_u32 s38, s28, 0x44800000
	v_add_u32_e32 v5, v3, v5
	v_lshlrev_b32_e32 v7, 3, v4
	s_addc_u32 s39, s29, 0
	v_readlane_b32 s3, v246, 10
	v_ashrrev_i32_e32 v6, 6, v5
	v_and_b32_e32 v7, -16, v7
	s_add_u32 s3, s28, s3
	v_add_u32_e32 v7, v6, v7
	s_addc_u32 s4, s29, 0
	v_and_b32_e32 v6, 3, v6
	s_mov_b32 s5, 0x3fffe0
	v_lshrrev_b32_e32 v8, 2, v7
	v_lshlrev_b32_e32 v9, 1, v7
	v_and_b32_e32 v5, 0xc0, v5
	s_add_u32 s60, s3, 0x4700000
	v_and_or_b32 v6, v7, s5, v6
	v_and_b32_e32 v8, 4, v8
	v_and_b32_e32 v9, 24, v9
	v_lshlrev_b32_e32 v4, 5, v4
	v_sub_u32_e32 v3, v3, v5
	s_addc_u32 s61, s4, 0
	v_or3_b32 v6, v6, v8, v9
	v_and_b32_e32 v4, 32, v4
	v_ashrrev_i16_sdwa v3, v223, sext(v3) dst_sel:DWORD dst_unused:UNUSED_PAD src0_sel:DWORD src1_sel:BYTE_0
	s_movk_i32 s4, 0xc00
	v_mul_u32_u24_e32 v6, 0xc00, v6
	v_add_u32_sdwa v3, v4, sext(v3) dst_sel:DWORD dst_unused:UNUSED_PAD src0_sel:DWORD src1_sel:WORD_0
	v_mul_lo_u32 v4, v7, s4
	v_add_lshl_u32 v176, v6, v3, 1
	v_add_lshl_u32 v178, v3, v4, 1
	v_bfe_i32 v3, v0, 27, 1
	v_lshrrev_b32_e32 v3, 22, v3
	v_add_u32_e32 v3, v2, v3
	v_and_b32_e32 v3, 0xfffffc00, v3
	v_sub_u32_e32 v2, v2, v3
	v_lshrrev_b32_e32 v3, 4, v2
	v_ashrrev_i32_e32 v5, 31, v0
	v_bitop3_b32 v2, v3, v2, 32 bitop3:0x6c
	v_lshrrev_b32_e32 v5, 26, v5
	v_ashrrev_i32_e32 v3, 31, v2
	v_add_u32_e32 v5, v0, v5
	v_lshrrev_b32_e32 v3, 26, v3
	v_ashrrev_i32_e32 v5, 6, v5
	v_add_u32_e32 v3, v2, v3
	v_lshlrev_b32_e32 v6, 3, v5
	v_ashrrev_i32_e32 v4, 6, v3
	v_and_b32_e32 v6, -16, v6
	v_add_u32_e32 v6, v4, v6
	v_and_b32_e32 v4, 3, v4
	v_and_b32_e32 v3, 0xc0, v3
	s_ashr_i32 s3, s2, 6
	v_and_or_b32 v4, v6, s5, v4
	v_lshrrev_b32_e32 v7, 2, v6
	v_lshlrev_b32_e32 v8, 1, v6
	v_sub_u32_e32 v2, v2, v3
	v_mul_lo_u32 v3, v6, s4
	v_readlane_b32 s4, v247, 4
	s_ashr_i32 s8, s2, 8
	s_lshl_b32 s62, s3, 10
	v_and_b32_e32 v7, 4, v7
	v_and_b32_e32 v8, 24, v8
	v_lshlrev_b32_e32 v5, 5, v5
	s_mov_b32 s10, s4
	s_mul_i32 s4, s4, 0x180000
	v_or3_b32 v4, v4, v7, v8
	v_and_b32_e32 v5, 32, v5
	v_ashrrev_i16_sdwa v2, v223, sext(v2) dst_sel:DWORD dst_unused:UNUSED_PAD src0_sel:DWORD src1_sel:BYTE_0
	s_add_u32 s12, s60, s4
	s_mul_hi_i32 s4, s10, 0x180000
	v_mul_u32_u24_e32 v4, 0xc00, v4
	v_add_u32_sdwa v2, v5, sext(v2) dst_sel:DWORD dst_unused:UNUSED_PAD src0_sel:DWORD src1_sel:WORD_0
	s_addc_u32 s13, s61, s4
	s_add_i32 s63, s62, 0
	v_add_lshl_u32 v180, v4, v2, 1
	s_add_i32 m0, s63, 0x10000
	v_readlane_b32 s5, v247, 5
	global_load_lds_dwordx4 v180, s[12:13]
	s_add_i32 m0, s63, 0x12000
	s_add_u32 s4, s12, 0xc0000
	global_load_lds_dwordx4 v176, s[12:13]
	s_addc_u32 s5, s13, 0
	s_add_i32 m0, s63, 0x14000
	v_add_lshl_u32 v182, v2, v3, 1
	global_load_lds_dwordx4 v180, s[4:5]
	s_add_i32 m0, s63, 0x16000
	v_mov_b32_e32 v181, v1
	global_load_lds_dwordx4 v176, s[4:5]
	v_readlane_b32 s4, v247, 0
	s_mov_b32 s10, s4
	s_mul_i32 s4, s4, 0x180000
	s_add_u32 s48, s38, s4
	s_mul_hi_i32 s4, s10, 0x180000
	s_addc_u32 s49, s39, s4
	s_add_i32 s64, s63, 0x2000
	v_readlane_b32 s5, v247, 1
	s_mov_b32 m0, s63
	s_add_u32 s4, s48, 0xc0000
	global_load_lds_dwordx4 v182, s[48:49]
	s_mov_b32 m0, s64
	s_addc_u32 s5, s49, 0
	s_add_i32 s65, s63, 0x4000
	global_load_lds_dwordx4 v178, s[48:49]
	s_mov_b32 m0, s65
	s_add_i32 s66, s63, 0x6000
	global_load_lds_dwordx4 v182, s[4:5]
	s_mov_b32 m0, s66
	v_mov_b32_e32 v177, v1
	global_load_lds_dwordx4 v178, s[4:5]
	v_mov_b32_e32 v183, v1
	v_mov_b32_e32 v179, v1
	s_cmp_eq_u32 s8, 1
	v_lshl_add_u64 v[8:9], s[12:13], 0, v[180:181]
	v_lshl_add_u64 v[6:7], s[12:13], 0, v[176:177]
	v_lshl_add_u64 v[2:3], s[48:49], 0, v[182:183]
	s_cselect_b64 s[4:5], -1, 0
	s_cmp_lg_u32 s8, 1
	v_lshl_add_u64 v[4:5], s[48:49], 0, v[178:179]
	s_cbranch_scc1 .LBB0_632
	s_barrier
